# non-temporal hint on the last-use residual-stream loads in the combine phase, on top of v60
# baseline (speedup 1.0000x reference)
.LBB0_1841:
	s_ashr_i32 s18, s0, 6
	s_add_i32 s10, s18, s77
	v_and_b32_e32 v1, 63, v0
	s_cmpk_lt_i32 s10, 0x4000
	s_cselect_b64 s[4:5], -1, 0
	s_cmpk_gt_i32 s10, 0x3fff
	v_lshlrev_b32_e32 v18, 3, v1
	s_waitcnt lgkmcnt(0)
	s_barrier
	s_cbranch_scc1 .LBB0_1843
	s_ashr_i32 s11, s10, 31
	s_lshl_b64 s[0:1], s[10:11], 11
	s_add_u32 s0, s6, s0
	s_addc_u32 s1, s7, s1
	v_mov_b32_e32 v19, v101
	v_lshl_add_u64 v[2:3], s[0:1], 0, v[18:19]
	s_mov_b64 s[0:1], 0x33000000
	v_lshl_add_u64 v[4:5], v[2:3], 0, s[0:1]
	s_mov_b32 s0, 0x33000000
	v_add_co_u32_e32 v2, vcc, s0, v2
	s_lshl_b64 s[0:1], s[10:11], 13
	s_add_u32 s0, s6, s0
	v_addc_co_u32_e32 v3, vcc, 0, v3, vcc
	s_addc_u32 s1, s7, s1
	global_load_dwordx2 v[156:157], v[4:5], off offset:1536 nt
	global_load_dwordx2 v[160:161], v[2:3], off nt
	global_load_dwordx2 v[158:159], v[4:5], off offset:1024 nt
	global_load_dwordx2 v[162:163], v[4:5], off offset:512 nt
	v_lshl_add_u64 v[2:3], s[0:1], 0, v[18:19]
	s_mov_b64 s[0:1], 0x54000000
	v_lshl_add_u64 v[4:5], v[2:3], 0, s[0:1]
	s_brev_b32 s0, 42
	v_add_co_u32_e32 v6, vcc, s0, v2
	s_nop 1
	v_addc_co_u32_e32 v7, vcc, 0, v3, vcc
	v_add_co_u32_e32 v2, vcc, 0x54001000, v2
	global_load_dwordx2 v[128:129], v[4:5], off offset:512 nt
	global_load_dwordx2 v[132:133], v[4:5], off offset:1024 nt
	global_load_dwordx2 v[136:137], v[4:5], off offset:1536 nt
	global_load_dwordx2 v[124:125], v[4:5], off offset:2048 nt
	global_load_dwordx2 v[126:127], v[6:7], off nt
	global_load_dwordx2 v[130:131], v[4:5], off offset:2560 nt
	global_load_dwordx2 v[134:135], v[4:5], off offset:3072 nt
	global_load_dwordx2 v[138:139], v[4:5], off offset:3584 nt
	v_addc_co_u32_e32 v3, vcc, 0, v3, vcc
	global_load_dwordx2 v[152:153], v[2:3], off nt
	global_load_dwordx2 v[148:149], v[2:3], off offset:512 nt
	global_load_dwordx2 v[144:145], v[2:3], off offset:1024 nt
	global_load_dwordx2 v[140:141], v[2:3], off offset:1536 nt
	global_load_dwordx2 v[154:155], v[2:3], off offset:2048 nt
	global_load_dwordx2 v[150:151], v[2:3], off offset:2560 nt
	global_load_dwordx2 v[146:147], v[2:3], off offset:3072 nt
	global_load_dwordx2 v[142:143], v[2:3], off offset:3584 nt

.LBB0_1860:
	s_add_i32 s10, s10, s86
	s_cmpk_gt_i32 s10, 0x3fff
	s_cselect_b64 s[14:15], -1, 0
	s_and_b64 vcc, exec, s[14:15]
	s_waitcnt vmcnt(17)
	v_mov_b64_e32 v[98:99], v[136:137]
	v_mov_b64_e32 v[94:95], v[132:133]
	v_mov_b64_e32 v[92:93], v[128:129]
	s_waitcnt vmcnt(15)
	v_mov_b64_e32 v[90:91], v[126:127]
	v_mov_b64_e32 v[104:105], v[124:125]
	s_waitcnt vmcnt(14)
	v_mov_b64_e32 v[108:109], v[130:131]
	s_waitcnt vmcnt(13)
	v_mov_b64_e32 v[112:113], v[134:135]
	s_waitcnt vmcnt(12)
	v_mov_b64_e32 v[116:117], v[138:139]
	s_waitcnt vmcnt(11)
	v_mov_b64_e32 v[96:97], v[152:153]
	s_waitcnt vmcnt(10)
	v_mov_b64_e32 v[102:103], v[148:149]
	s_waitcnt vmcnt(9)
	v_mov_b64_e32 v[106:107], v[144:145]
	s_waitcnt vmcnt(8)
	v_mov_b64_e32 v[110:111], v[140:141]
	s_waitcnt vmcnt(7)
	v_mov_b64_e32 v[114:115], v[154:155]
	s_waitcnt vmcnt(6)
	v_mov_b64_e32 v[118:119], v[150:151]
	s_waitcnt vmcnt(5)
	v_mov_b64_e32 v[120:121], v[146:147]
	s_waitcnt vmcnt(4)
	v_mov_b64_e32 v[122:123], v[142:143]
	v_mov_b64_e32 v[88:89], v[160:161]
	v_mov_b64_e32 v[86:87], v[162:163]
	v_mov_b64_e32 v[84:85], v[158:159]
	v_mov_b64_e32 v[82:83], v[156:157]
	s_cbranch_vccnz .LBB0_1862
	v_lshl_add_u64 v[82:83], s[6:7], 0, v[80:81]
	v_add_co_u32_e32 v88, vcc, 0x33000000, v82
	v_lshl_add_u64 v[96:97], s[6:7], 0, v[78:79]
	s_nop 0
	v_addc_co_u32_e32 v89, vcc, 0, v83, vcc
	v_add_co_u32_e32 v102, vcc, 0x54000000, v96
	global_load_dwordx2 v[82:83], v[88:89], off offset:1536 nt
	global_load_dwordx2 v[84:85], v[88:89], off offset:1024 nt
	global_load_dwordx2 v[86:87], v[88:89], off offset:512 nt
	s_nop 0
	global_load_dwordx2 v[88:89], v[88:89], off nt
	v_addc_co_u32_e32 v103, vcc, 0, v97, vcc
	v_add_co_u32_e32 v122, vcc, 0x54001000, v96
	global_load_dwordx2 v[90:91], v[102:103], off nt
	global_load_dwordx2 v[92:93], v[102:103], off offset:512 nt
	global_load_dwordx2 v[94:95], v[102:103], off offset:1024 nt
	global_load_dwordx2 v[98:99], v[102:103], off offset:1536 nt
	global_load_dwordx2 v[104:105], v[102:103], off offset:2048 nt
	global_load_dwordx2 v[108:109], v[102:103], off offset:2560 nt
	global_load_dwordx2 v[112:113], v[102:103], off offset:3072 nt
	global_load_dwordx2 v[116:117], v[102:103], off offset:3584 nt
	v_addc_co_u32_e32 v123, vcc, 0, v97, vcc
	global_load_dwordx2 v[96:97], v[122:123], off nt
	global_load_dwordx2 v[102:103], v[122:123], off offset:512 nt
	global_load_dwordx2 v[106:107], v[122:123], off offset:1024 nt
	global_load_dwordx2 v[110:111], v[122:123], off offset:1536 nt
	global_load_dwordx2 v[114:115], v[122:123], off offset:2048 nt
	global_load_dwordx2 v[118:119], v[122:123], off offset:2560 nt
	global_load_dwordx2 v[120:121], v[122:123], off offset:3072 nt
	s_nop 0
	global_load_dwordx2 v[122:123], v[122:123], off offset:3584 nt
